# GEMM kernels: the duplicate accumulator zeroing in front of each unit K loop moved onto its never-taken zero-trip branch
# speedup vs baseline: 1.0059x; 1.0059x over previous
.LBB2_19:
	v_mov_b32_e32 v129, 0
	s_andn2_b64 vcc, exec, s[24:25]
	s_cbranch_vccnz .Lz_g0_stub
	s_add_u32 s63, s26, 0x100
	s_addc_u32 s64, s27, 0
	s_add_u32 s26, s28, 0x80
	v_mov_b32_e32 v2, 0
	s_addc_u32 s27, s29, 0
	s_mov_b32 s28, 0
	v_mov_b32_e32 v3, v2
	v_mov_b32_e32 v4, v2
	v_mov_b32_e32 v5, v2
	v_mov_b32_e32 v6, v2
	v_mov_b32_e32 v7, v2
	v_mov_b32_e32 v8, v2
	v_mov_b32_e32 v9, v2
	v_mov_b32_e32 v18, v2
	v_mov_b32_e32 v19, v2
	v_mov_b32_e32 v20, v2
	v_mov_b32_e32 v21, v2
	v_mov_b32_e32 v22, v2
	v_mov_b32_e32 v23, v2
	v_mov_b32_e32 v24, v2
	v_mov_b32_e32 v25, v2
	v_mov_b32_e32 v34, v2
	v_mov_b32_e32 v35, v2
	v_mov_b32_e32 v36, v2
	v_mov_b32_e32 v37, v2
	v_mov_b32_e32 v38, v2
	v_mov_b32_e32 v39, v2
	v_mov_b32_e32 v40, v2
	v_mov_b32_e32 v41, v2
	v_mov_b32_e32 v50, v2
	v_mov_b32_e32 v51, v2
	v_mov_b32_e32 v52, v2
	v_mov_b32_e32 v53, v2
	v_mov_b32_e32 v54, v2
	v_mov_b32_e32 v55, v2
	v_mov_b32_e32 v56, v2
	v_mov_b32_e32 v57, v2
	v_mov_b32_e32 v10, v2
	v_mov_b32_e32 v11, v2
	v_mov_b32_e32 v12, v2
	v_mov_b32_e32 v13, v2
	v_mov_b32_e32 v14, v2
	v_mov_b32_e32 v15, v2
	v_mov_b32_e32 v16, v2
	v_mov_b32_e32 v17, v2
	v_mov_b32_e32 v26, v2
	v_mov_b32_e32 v27, v2
	v_mov_b32_e32 v28, v2
	v_mov_b32_e32 v29, v2
	v_mov_b32_e32 v30, v2
	v_mov_b32_e32 v31, v2
	v_mov_b32_e32 v32, v2
	v_mov_b32_e32 v33, v2
	v_mov_b32_e32 v42, v2
	v_mov_b32_e32 v43, v2
	v_mov_b32_e32 v44, v2
	v_mov_b32_e32 v45, v2
	v_mov_b32_e32 v46, v2
	v_mov_b32_e32 v47, v2
	v_mov_b32_e32 v48, v2
	v_mov_b32_e32 v49, v2
	v_mov_b32_e32 v58, v2
	v_mov_b32_e32 v59, v2
	v_mov_b32_e32 v60, v2
	v_mov_b32_e32 v61, v2
	v_mov_b32_e32 v62, v2
	v_mov_b32_e32 v63, v2
	v_mov_b32_e32 v64, v2
	v_mov_b32_e32 v65, v2
	v_mov_b32_e32 v66, v2
	v_mov_b32_e32 v67, v2
	v_mov_b32_e32 v68, v2
	v_mov_b32_e32 v69, v2
	v_mov_b32_e32 v70, v2
	v_mov_b32_e32 v71, v2
	v_mov_b32_e32 v72, v2
	v_mov_b32_e32 v73, v2
	v_mov_b32_e32 v82, v2
	v_mov_b32_e32 v83, v2
	v_mov_b32_e32 v84, v2
	v_mov_b32_e32 v85, v2
	v_mov_b32_e32 v86, v2
	v_mov_b32_e32 v87, v2
	v_mov_b32_e32 v88, v2
	v_mov_b32_e32 v89, v2
	v_mov_b32_e32 v98, v2
	v_mov_b32_e32 v99, v2
	v_mov_b32_e32 v100, v2
	v_mov_b32_e32 v101, v2
	v_mov_b32_e32 v102, v2
	v_mov_b32_e32 v103, v2
	v_mov_b32_e32 v104, v2
	v_mov_b32_e32 v105, v2
	v_mov_b32_e32 v114, v2
	v_mov_b32_e32 v115, v2
	v_mov_b32_e32 v116, v2
	v_mov_b32_e32 v117, v2
	v_mov_b32_e32 v118, v2
	v_mov_b32_e32 v119, v2
	v_mov_b32_e32 v120, v2
	v_mov_b32_e32 v121, v2
	v_mov_b32_e32 v74, v2
	v_mov_b32_e32 v75, v2
	v_mov_b32_e32 v76, v2
	v_mov_b32_e32 v77, v2
	v_mov_b32_e32 v78, v2
	v_mov_b32_e32 v79, v2
	v_mov_b32_e32 v80, v2
	v_mov_b32_e32 v81, v2
	v_mov_b32_e32 v90, v2
	v_mov_b32_e32 v91, v2
	v_mov_b32_e32 v92, v2
	v_mov_b32_e32 v93, v2
	v_mov_b32_e32 v94, v2
	v_mov_b32_e32 v95, v2
	v_mov_b32_e32 v96, v2
	v_mov_b32_e32 v97, v2
	v_mov_b32_e32 v106, v2
	v_mov_b32_e32 v107, v2
	v_mov_b32_e32 v108, v2
	v_mov_b32_e32 v109, v2
	v_mov_b32_e32 v110, v2
	v_mov_b32_e32 v111, v2
	v_mov_b32_e32 v112, v2
	v_mov_b32_e32 v113, v2
	v_mov_b32_e32 v122, v2
	v_mov_b32_e32 v123, v2
	v_mov_b32_e32 v124, v2
	v_mov_b32_e32 v125, v2
	v_mov_b32_e32 v126, v2
	v_mov_b32_e32 v127, v2
	v_mov_b32_e32 v128, v2
	v_mov_b32_e32 v129, v2

.Lz_g0_stub:
	v_mov_b32_e32 v128, v129
	v_mov_b32_e32 v127, v129
	v_mov_b32_e32 v126, v129
	v_mov_b32_e32 v125, v129
	v_mov_b32_e32 v124, v129
	v_mov_b32_e32 v123, v129
	v_mov_b32_e32 v122, v129
	v_mov_b32_e32 v113, v129
	v_mov_b32_e32 v112, v129
	v_mov_b32_e32 v111, v129
	v_mov_b32_e32 v110, v129
	v_mov_b32_e32 v109, v129
	v_mov_b32_e32 v108, v129
	v_mov_b32_e32 v107, v129
	v_mov_b32_e32 v106, v129
	v_mov_b32_e32 v97, v129
	v_mov_b32_e32 v96, v129
	v_mov_b32_e32 v95, v129
	v_mov_b32_e32 v94, v129
	v_mov_b32_e32 v93, v129
	v_mov_b32_e32 v92, v129
	v_mov_b32_e32 v91, v129
	v_mov_b32_e32 v90, v129
	v_mov_b32_e32 v81, v129
	v_mov_b32_e32 v80, v129
	v_mov_b32_e32 v79, v129
	v_mov_b32_e32 v78, v129
	v_mov_b32_e32 v77, v129
	v_mov_b32_e32 v76, v129
	v_mov_b32_e32 v75, v129
	v_mov_b32_e32 v74, v129
	v_mov_b32_e32 v121, v129
	v_mov_b32_e32 v120, v129
	v_mov_b32_e32 v119, v129
	v_mov_b32_e32 v118, v129
	v_mov_b32_e32 v117, v129
	v_mov_b32_e32 v116, v129
	v_mov_b32_e32 v115, v129
	v_mov_b32_e32 v114, v129
	v_mov_b32_e32 v105, v129
	v_mov_b32_e32 v104, v129
	v_mov_b32_e32 v103, v129
	v_mov_b32_e32 v102, v129
	v_mov_b32_e32 v101, v129
	v_mov_b32_e32 v100, v129
	v_mov_b32_e32 v99, v129
	v_mov_b32_e32 v98, v129
	v_mov_b32_e32 v89, v129
	v_mov_b32_e32 v88, v129
	v_mov_b32_e32 v87, v129
	v_mov_b32_e32 v86, v129
	v_mov_b32_e32 v85, v129
	v_mov_b32_e32 v84, v129
	v_mov_b32_e32 v83, v129
	v_mov_b32_e32 v82, v129
	v_mov_b32_e32 v73, v129
	v_mov_b32_e32 v72, v129
	v_mov_b32_e32 v71, v129
	v_mov_b32_e32 v70, v129
	v_mov_b32_e32 v69, v129
	v_mov_b32_e32 v68, v129
	v_mov_b32_e32 v67, v129
	v_mov_b32_e32 v66, v129
	v_mov_b32_e32 v65, v129
	v_mov_b32_e32 v64, v129
	v_mov_b32_e32 v63, v129
	v_mov_b32_e32 v62, v129
	v_mov_b32_e32 v61, v129
	v_mov_b32_e32 v60, v129
	v_mov_b32_e32 v59, v129
	v_mov_b32_e32 v58, v129
	v_mov_b32_e32 v49, v129
	v_mov_b32_e32 v48, v129
	v_mov_b32_e32 v47, v129
	v_mov_b32_e32 v46, v129
	v_mov_b32_e32 v45, v129
	v_mov_b32_e32 v44, v129
	v_mov_b32_e32 v43, v129
	v_mov_b32_e32 v42, v129
	v_mov_b32_e32 v33, v129
	v_mov_b32_e32 v32, v129
	v_mov_b32_e32 v31, v129
	v_mov_b32_e32 v30, v129
	v_mov_b32_e32 v29, v129
	v_mov_b32_e32 v28, v129
	v_mov_b32_e32 v27, v129
	v_mov_b32_e32 v26, v129
	v_mov_b32_e32 v17, v129
	v_mov_b32_e32 v16, v129
	v_mov_b32_e32 v15, v129
	v_mov_b32_e32 v14, v129
	v_mov_b32_e32 v13, v129
	v_mov_b32_e32 v12, v129
	v_mov_b32_e32 v11, v129
	v_mov_b32_e32 v10, v129
	v_mov_b32_e32 v57, v129
	v_mov_b32_e32 v56, v129
	v_mov_b32_e32 v55, v129
	v_mov_b32_e32 v54, v129
	v_mov_b32_e32 v53, v129
	v_mov_b32_e32 v52, v129
	v_mov_b32_e32 v51, v129
	v_mov_b32_e32 v50, v129
	v_mov_b32_e32 v41, v129
	v_mov_b32_e32 v40, v129
	v_mov_b32_e32 v39, v129
	v_mov_b32_e32 v38, v129
	v_mov_b32_e32 v37, v129
	v_mov_b32_e32 v36, v129
	v_mov_b32_e32 v35, v129
	v_mov_b32_e32 v34, v129
	v_mov_b32_e32 v25, v129
	v_mov_b32_e32 v24, v129
	v_mov_b32_e32 v23, v129
	v_mov_b32_e32 v22, v129
	v_mov_b32_e32 v21, v129
	v_mov_b32_e32 v20, v129
	v_mov_b32_e32 v19, v129
	v_mov_b32_e32 v18, v129
	v_mov_b32_e32 v9, v129
	v_mov_b32_e32 v8, v129
	v_mov_b32_e32 v7, v129
	v_mov_b32_e32 v6, v129
	v_mov_b32_e32 v5, v129
	v_mov_b32_e32 v4, v129
	v_mov_b32_e32 v3, v129
	v_mov_b32_e32 v2, v129
	s_branch .LBB2_8

.LBB3_21:
	v_mov_b32_e32 v119, 0
	s_andn2_b64 vcc, exec, s[26:27]
	s_cbranch_vccnz .Lz_g1_stub
	s_add_u32 s69, s30, 0x100
	s_addc_u32 s70, s31, 0
	s_add_u32 s30, s34, 0x80
	v_mov_b32_e32 v0, 0
	s_addc_u32 s31, s35, 0
	s_mov_b32 s34, 0
	v_mov_b32_e32 v1, v0
	v_mov_b32_e32 v2, v0
	v_mov_b32_e32 v3, v0
	v_mov_b32_e32 v4, v0
	v_mov_b32_e32 v5, v0
	v_mov_b32_e32 v6, v0
	v_mov_b32_e32 v7, v0
	v_mov_b32_e32 v16, v0
	v_mov_b32_e32 v17, v0
	v_mov_b32_e32 v18, v0
	v_mov_b32_e32 v19, v0
	v_mov_b32_e32 v20, v0
	v_mov_b32_e32 v21, v0
	v_mov_b32_e32 v22, v0
	v_mov_b32_e32 v23, v0
	v_mov_b32_e32 v32, v0
	v_mov_b32_e32 v33, v0
	v_mov_b32_e32 v34, v0
	v_mov_b32_e32 v35, v0
	v_mov_b32_e32 v36, v0
	v_mov_b32_e32 v37, v0
	v_mov_b32_e32 v38, v0
	v_mov_b32_e32 v39, v0
	v_mov_b32_e32 v48, v0
	v_mov_b32_e32 v49, v0
	v_mov_b32_e32 v50, v0
	v_mov_b32_e32 v51, v0
	v_mov_b32_e32 v52, v0
	v_mov_b32_e32 v53, v0
	v_mov_b32_e32 v54, v0
	v_mov_b32_e32 v55, v0
	v_mov_b32_e32 v8, v0
	v_mov_b32_e32 v9, v0
	v_mov_b32_e32 v10, v0
	v_mov_b32_e32 v11, v0
	v_mov_b32_e32 v12, v0
	v_mov_b32_e32 v13, v0
	v_mov_b32_e32 v14, v0
	v_mov_b32_e32 v15, v0
	v_mov_b32_e32 v24, v0
	v_mov_b32_e32 v25, v0
	v_mov_b32_e32 v26, v0
	v_mov_b32_e32 v27, v0
	v_mov_b32_e32 v28, v0
	v_mov_b32_e32 v29, v0
	v_mov_b32_e32 v30, v0
	v_mov_b32_e32 v31, v0
	v_mov_b32_e32 v40, v0
	v_mov_b32_e32 v41, v0
	v_mov_b32_e32 v42, v0
	v_mov_b32_e32 v43, v0
	v_mov_b32_e32 v44, v0
	v_mov_b32_e32 v45, v0
	v_mov_b32_e32 v46, v0
	v_mov_b32_e32 v47, v0
	v_mov_b32_e32 v56, v0
	v_mov_b32_e32 v57, v0
	v_mov_b32_e32 v58, v0
	v_mov_b32_e32 v59, v0
	v_mov_b32_e32 v60, v0
	v_mov_b32_e32 v61, v0
	v_mov_b32_e32 v62, v0
	v_mov_b32_e32 v63, v0
	v_mov_b32_e32 v64, v0
	v_mov_b32_e32 v65, v0
	v_mov_b32_e32 v66, v0
	v_mov_b32_e32 v67, v0
	v_mov_b32_e32 v68, v0
	v_mov_b32_e32 v69, v0
	v_mov_b32_e32 v70, v0
	v_mov_b32_e32 v71, v0
	v_mov_b32_e32 v80, v0
	v_mov_b32_e32 v81, v0
	v_mov_b32_e32 v82, v0
	v_mov_b32_e32 v83, v0
	v_mov_b32_e32 v84, v0
	v_mov_b32_e32 v85, v0
	v_mov_b32_e32 v86, v0
	v_mov_b32_e32 v87, v0
	v_mov_b32_e32 v96, v0
	v_mov_b32_e32 v97, v0
	v_mov_b32_e32 v98, v0
	v_mov_b32_e32 v99, v0
	v_mov_b32_e32 v100, v0
	v_mov_b32_e32 v101, v0
	v_mov_b32_e32 v102, v0
	v_mov_b32_e32 v103, v0
	v_mov_b32_e32 v112, v0
	v_mov_b32_e32 v113, v0
	v_mov_b32_e32 v114, v0
	v_mov_b32_e32 v115, v0
	v_mov_b32_e32 v120, v0
	v_mov_b32_e32 v121, v0
	v_mov_b32_e32 v122, v0
	v_mov_b32_e32 v123, v0
	v_mov_b32_e32 v72, v0
	v_mov_b32_e32 v73, v0
	v_mov_b32_e32 v74, v0
	v_mov_b32_e32 v75, v0
	v_mov_b32_e32 v76, v0
	v_mov_b32_e32 v77, v0
	v_mov_b32_e32 v78, v0
	v_mov_b32_e32 v79, v0
	v_mov_b32_e32 v88, v0
	v_mov_b32_e32 v89, v0
	v_mov_b32_e32 v90, v0
	v_mov_b32_e32 v91, v0
	v_mov_b32_e32 v92, v0
	v_mov_b32_e32 v93, v0
	v_mov_b32_e32 v94, v0
	v_mov_b32_e32 v95, v0
	v_mov_b32_e32 v104, v0
	v_mov_b32_e32 v105, v0
	v_mov_b32_e32 v106, v0
	v_mov_b32_e32 v107, v0
	v_mov_b32_e32 v108, v0
	v_mov_b32_e32 v109, v0
	v_mov_b32_e32 v110, v0
	v_mov_b32_e32 v111, v0
	v_mov_b32_e32 v124, v0
	v_mov_b32_e32 v125, v0
	v_mov_b32_e32 v126, v0
	v_mov_b32_e32 v127, v0
	v_mov_b32_e32 v116, v0
	v_mov_b32_e32 v117, v0
	v_mov_b32_e32 v118, v0
	v_mov_b32_e32 v119, v0

.Lz_g1_stub:
	v_mov_b32_e32 v118, v119
	v_mov_b32_e32 v117, v119
	v_mov_b32_e32 v116, v119
	v_mov_b32_e32 v127, v119
	v_mov_b32_e32 v126, v119
	v_mov_b32_e32 v125, v119
	v_mov_b32_e32 v124, v119
	v_mov_b32_e32 v111, v119
	v_mov_b32_e32 v110, v119
	v_mov_b32_e32 v109, v119
	v_mov_b32_e32 v108, v119
	v_mov_b32_e32 v107, v119
	v_mov_b32_e32 v106, v119
	v_mov_b32_e32 v105, v119
	v_mov_b32_e32 v104, v119
	v_mov_b32_e32 v95, v119
	v_mov_b32_e32 v94, v119
	v_mov_b32_e32 v93, v119
	v_mov_b32_e32 v92, v119
	v_mov_b32_e32 v91, v119
	v_mov_b32_e32 v90, v119
	v_mov_b32_e32 v89, v119
	v_mov_b32_e32 v88, v119
	v_mov_b32_e32 v79, v119
	v_mov_b32_e32 v78, v119
	v_mov_b32_e32 v77, v119
	v_mov_b32_e32 v76, v119
	v_mov_b32_e32 v75, v119
	v_mov_b32_e32 v74, v119
	v_mov_b32_e32 v73, v119
	v_mov_b32_e32 v72, v119
	v_mov_b32_e32 v123, v119
	v_mov_b32_e32 v122, v119
	v_mov_b32_e32 v121, v119
	v_mov_b32_e32 v120, v119
	v_mov_b32_e32 v115, v119
	v_mov_b32_e32 v114, v119
	v_mov_b32_e32 v113, v119
	v_mov_b32_e32 v112, v119
	v_mov_b32_e32 v103, v119
	v_mov_b32_e32 v102, v119
	v_mov_b32_e32 v101, v119
	v_mov_b32_e32 v100, v119
	v_mov_b32_e32 v99, v119
	v_mov_b32_e32 v98, v119
	v_mov_b32_e32 v97, v119
	v_mov_b32_e32 v96, v119
	v_mov_b32_e32 v87, v119
	v_mov_b32_e32 v86, v119
	v_mov_b32_e32 v85, v119
	v_mov_b32_e32 v84, v119
	v_mov_b32_e32 v83, v119
	v_mov_b32_e32 v82, v119
	v_mov_b32_e32 v81, v119
	v_mov_b32_e32 v80, v119
	v_mov_b32_e32 v71, v119
	v_mov_b32_e32 v70, v119
	v_mov_b32_e32 v69, v119
	v_mov_b32_e32 v68, v119
	v_mov_b32_e32 v67, v119
	v_mov_b32_e32 v66, v119
	v_mov_b32_e32 v65, v119
	v_mov_b32_e32 v64, v119
	v_mov_b32_e32 v63, v119
	v_mov_b32_e32 v62, v119
	v_mov_b32_e32 v61, v119
	v_mov_b32_e32 v60, v119
	v_mov_b32_e32 v59, v119
	v_mov_b32_e32 v58, v119
	v_mov_b32_e32 v57, v119
	v_mov_b32_e32 v56, v119
	v_mov_b32_e32 v47, v119
	v_mov_b32_e32 v46, v119
	v_mov_b32_e32 v45, v119
	v_mov_b32_e32 v44, v119
	v_mov_b32_e32 v43, v119
	v_mov_b32_e32 v42, v119
	v_mov_b32_e32 v41, v119
	v_mov_b32_e32 v40, v119
	v_mov_b32_e32 v31, v119
	v_mov_b32_e32 v30, v119
	v_mov_b32_e32 v29, v119
	v_mov_b32_e32 v28, v119
	v_mov_b32_e32 v27, v119
	v_mov_b32_e32 v26, v119
	v_mov_b32_e32 v25, v119
	v_mov_b32_e32 v24, v119
	v_mov_b32_e32 v15, v119
	v_mov_b32_e32 v14, v119
	v_mov_b32_e32 v13, v119
	v_mov_b32_e32 v12, v119
	v_mov_b32_e32 v11, v119
	v_mov_b32_e32 v10, v119
	v_mov_b32_e32 v9, v119
	v_mov_b32_e32 v8, v119
	v_mov_b32_e32 v55, v119
	v_mov_b32_e32 v54, v119
	v_mov_b32_e32 v53, v119
	v_mov_b32_e32 v52, v119
	v_mov_b32_e32 v51, v119
	v_mov_b32_e32 v50, v119
	v_mov_b32_e32 v49, v119
	v_mov_b32_e32 v48, v119
	v_mov_b32_e32 v39, v119
	v_mov_b32_e32 v38, v119
	v_mov_b32_e32 v37, v119
	v_mov_b32_e32 v36, v119
	v_mov_b32_e32 v35, v119
	v_mov_b32_e32 v34, v119
	v_mov_b32_e32 v33, v119
	v_mov_b32_e32 v32, v119
	v_mov_b32_e32 v23, v119
	v_mov_b32_e32 v22, v119
	v_mov_b32_e32 v21, v119
	v_mov_b32_e32 v20, v119
	v_mov_b32_e32 v19, v119
	v_mov_b32_e32 v18, v119
	v_mov_b32_e32 v17, v119
	v_mov_b32_e32 v16, v119
	v_mov_b32_e32 v7, v119
	v_mov_b32_e32 v6, v119
	v_mov_b32_e32 v5, v119
	v_mov_b32_e32 v4, v119
	v_mov_b32_e32 v3, v119
	v_mov_b32_e32 v2, v119
	v_mov_b32_e32 v1, v119
	v_mov_b32_e32 v0, v119
	s_branch .LBB3_10
